# merge GEMM chain unit order: 8 row tiles x 4 col tiles per XCD round with the column block rotated by XCD index (weight panels shared by 8 workgroups, XCDs decorrelated)
# speedup vs baseline: 1.0103x; 1.0014x over previous
.LBB0_2047:
	s_lshr_b32 s8, s45, 5
	s_and_b32 s9, s45, 31
	s_lshr_b32 s18, s8, 1
	s_lshl_b32 s18, s18, 3
	s_and_b32 s19, s9, 7
	s_add_i32 s19, s19, s18
	v_readlane_b32 s21, v252, 34
	s_lshr_b32 s18, s21, 4
	s_add_i32 s18, s18, s8
	s_and_b32 s18, s18, 1
	s_lshl_b32 s18, s18, 2
	s_lshr_b32 s9, s9, 3
	s_add_i32 s18, s18, s9
	s_add_i32 s19, s19, s21
	v_readlane_b32 s8, v252, 61
	s_lshl_b32 s46, s19, 8
	s_lshl_b32 s10, s18, 7
	s_add_i32 s45, s45, s8
	s_lshr_b32 s8, s45, 5
	s_and_b32 s9, s45, 31
	s_lshr_b32 s11, s8, 1
	s_lshl_b32 s11, s11, 3
	s_and_b32 s20, s9, 7
	s_add_i32 s20, s20, s11
	s_add_i32 s20, s20, s21
	s_lshr_b32 s11, s21, 4
	s_add_i32 s11, s11, s8
	s_and_b32 s11, s11, 1
	s_lshl_b32 s11, s11, 2
	s_lshr_b32 s9, s9, 3
	s_add_i32 s11, s11, s9
	s_cmpk_lt_i32 s45, 0x80
	s_cselect_b64 s[14:15], -1, 0
	s_cmpk_gt_i32 s45, 0x7f
	s_cselect_b64 s[8:9], -1, 0
	s_mul_i32 s49, s19, 0x240000
	s_lshl_b32 s52, s19, 2
	s_ashr_i32 s19, s18, 31
	s_lshl_b32 s47, s20, 8
	s_lshl_b32 s48, s11, 7
	s_ashr_i32 s11, s10, 31
	s_lshl_b64 s[18:19], s[18:19], 15
	s_waitcnt lgkmcnt(0)
	s_add_u32 s53, s2, s18
	v_mov_b32_e32 v68, 0
	s_addc_u32 s54, s3, s19
	s_mov_b32 s55, 0
	v_mov_b32_e32 v69, v68
	v_mov_b32_e32 v70, v68
	v_mov_b32_e32 v71, v68
	v_mov_b32_e32 v72, v68
	v_mov_b32_e32 v73, v68
	v_mov_b32_e32 v74, v68
	v_mov_b32_e32 v75, v68
	v_mov_b32_e32 v76, v68
	v_mov_b32_e32 v77, v68
	v_mov_b32_e32 v78, v68
	v_mov_b32_e32 v79, v68
	v_mov_b32_e32 v80, v68
	v_mov_b32_e32 v81, v68
	v_mov_b32_e32 v82, v68
	v_mov_b32_e32 v83, v68
	v_mov_b32_e32 v84, v68
	v_mov_b32_e32 v85, v68
	v_mov_b32_e32 v86, v68
	v_mov_b32_e32 v87, v68
	v_mov_b32_e32 v88, v68
	v_mov_b32_e32 v89, v68
	v_mov_b32_e32 v90, v68
	v_mov_b32_e32 v91, v68
	v_mov_b32_e32 v92, v68
	v_mov_b32_e32 v93, v68
	v_mov_b32_e32 v94, v68
	v_mov_b32_e32 v95, v68
	v_mov_b32_e32 v96, v68
	v_mov_b32_e32 v97, v68
	v_mov_b32_e32 v98, v68
	v_mov_b32_e32 v99, v68
	v_mov_b32_e32 v100, v68
	v_mov_b32_e32 v101, v68
	v_mov_b32_e32 v102, v68
	v_mov_b32_e32 v103, v68
	v_mov_b32_e32 v104, v68
	v_mov_b32_e32 v105, v68
	v_mov_b32_e32 v106, v68
	v_mov_b32_e32 v107, v68
	v_mov_b32_e32 v108, v68
	v_mov_b32_e32 v109, v68
	v_mov_b32_e32 v110, v68
	v_mov_b32_e32 v111, v68
	v_mov_b32_e32 v112, v68
	v_mov_b32_e32 v113, v68
	v_mov_b32_e32 v114, v68
	v_mov_b32_e32 v115, v68
	v_mov_b32_e32 v116, v68
	v_mov_b32_e32 v117, v68
	v_mov_b32_e32 v118, v68
	v_mov_b32_e32 v119, v68
	v_mov_b32_e32 v120, v68
	v_mov_b32_e32 v121, v68
	v_mov_b32_e32 v122, v68
	v_mov_b32_e32 v123, v68
	v_mov_b32_e32 v124, v68
	v_mov_b32_e32 v125, v68
	v_mov_b32_e32 v126, v68
	v_mov_b32_e32 v127, v68
	v_mov_b32_e32 v128, v68
	v_mov_b32_e32 v129, v68
	v_mov_b32_e32 v130, v68
	v_mov_b32_e32 v131, v68
	s_branch .LBB0_2049
